# union 7: expert GEMM1 epilogue gate loads issued together at the epilogue top, counted waits
# baseline (speedup 1.0000x reference)
.LBB0_1044:
	s_lshl_b32 s4, s10, 2
	s_add_i32 s4, s4, 0
	s_add_i32 s4, s4, 0x20180
	v_mov_b32_e32 v2, v177
	v_mov_b32_e32 v4, v192
	v_mov_b32_e32 v3, s4
	s_nop 15
	s_nop 15
	ds_read_b32 v10, v3
	s_cmp_lt_i32 s10, 64
	v_add_u32_e32 v11, s53, v2
	v_mov_b32_e32 v9, 0x3b800000
	s_cselect_b64 s[38:39], -1, 0
	s_cmp_gt_i32 s10, 63
	v_mov_b32_e32 v5, 0x3b800000
	s_cbranch_scc1 .LBB0_1048
	s_ashr_i32 s11, s10, 31
	s_lshl_b64 s[40:41], s[10:11], 15
	s_add_u32 s40, s51, s40
	s_addc_u32 s41, s52, s41
	v_add_u32_e32 v254, s14, v11
	v_lshlrev_b32_e32 v254, 2, v254
	global_load_dword v246, v254, s[40:41]
	global_load_dword v247, v254, s[40:41] offset:64
	global_load_dword v248, v254, s[40:41] offset:128
	global_load_dword v249, v254, s[40:41] offset:192
	global_load_dword v250, v254, s[40:41] offset:512
	global_load_dword v251, v254, s[40:41] offset:576
	global_load_dword v252, v254, s[40:41] offset:640
	global_load_dword v253, v254, s[40:41] offset:704
	v_add_u32_e32 v2, s14, v11
	s_waitcnt lgkmcnt(0)
	v_cmp_lt_i32_e32 vcc, v2, v10
	v_mov_b32_e32 v5, 0
	s_and_saveexec_b64 s[4:5], vcc
	s_cbranch_execz .LBB0_1047
	s_ashr_i32 s11, s10, 31
	s_lshl_b64 s[40:41], s[10:11], 15
	s_add_u32 s40, s51, s40
	s_addc_u32 s41, s52, s41
	v_ashrrev_i32_e32 v3, 31, v2
	v_lshl_add_u64 v[2:3], v[2:3], 2, s[40:41]
	s_waitcnt vmcnt(7)
	v_mul_f32_e32 v5, 0x3b800000, v246

.LBB0_1048:
	v_mul_f32_e32 v3, 0xbcb8aa3b, v158
	v_exp_f32_e32 v7, v3
	v_mul_f32_e32 v173, v158, v5
	v_mul_f32_e32 v12, 0xbcb8aa3b, v154
	v_add_f32_e32 v6, 1.0, v7
	v_rcp_f32_e32 v7, v6
	v_exp_f32_e32 v12, v12
	v_mul_f32_e32 v7, v7, v173
	v_mul_f32_e32 v173, v154, v5
	v_mul_f32_e32 v14, v150, v7
	v_add_f32_e32 v6, 1.0, v12
	v_rcp_f32_e32 v7, v6
	v_mul_f32_e32 v12, 0xbcb8aa3b, v159
	v_exp_f32_e32 v12, v12
	v_mul_f32_e32 v7, v7, v173
	v_mul_f32_e32 v173, v159, v5
	v_mul_f32_e32 v15, v146, v7
	v_add_f32_e32 v6, 1.0, v12
	v_rcp_f32_e32 v7, v6
	v_mul_f32_e32 v6, 0xbcb8aa3b, v155
	v_exp_f32_e32 v12, v6
	v_mul_f32_e32 v7, v7, v173
	v_mul_f32_e32 v173, v155, v5
	v_add_f32_e32 v8, 1.0, v12
	v_rcp_f32_e32 v13, v8
	v_mul_f32_e32 v8, v151, v7
	v_mul_f32_e32 v7, v13, v173
	v_mul_f32_e32 v13, 0xbcb8aa3b, v160
	v_exp_f32_e32 v13, v13
	v_mul_f32_e32 v16, v147, v7
	v_mul_f32_e32 v173, v160, v5
	v_mul_f32_e32 v12, 0xbcb8aa3b, v156
	v_add_f32_e32 v6, 1.0, v13
	v_rcp_f32_e32 v7, v6
	v_exp_f32_e32 v12, v12
	v_mul_f32_e32 v7, v7, v173
	v_mul_f32_e32 v173, v156, v5
	v_mul_f32_e32 v18, v152, v7
	v_add_f32_e32 v6, 1.0, v12
	v_rcp_f32_e32 v7, v6
	v_mul_f32_e32 v13, 0xbcb8aa3b, v161
	v_exp_f32_e32 v13, v13
	v_mul_f32_e32 v7, v7, v173
	v_mul_f32_e32 v173, v161, v5
	v_mul_f32_e32 v17, v148, v7
	v_add_f32_e32 v6, 1.0, v13
	v_rcp_f32_e32 v7, v6
	v_mul_f32_e32 v6, 0xbcb8aa3b, v157
	v_exp_f32_e32 v13, v6
	v_mul_f32_e32 v7, v7, v173
	v_mul_f32_e32 v173, v157, v5
	v_add_f32_e32 v12, 1.0, v13
	v_rcp_f32_e32 v13, v12
	v_mul_f32_e32 v20, v153, v7
	v_med3_f32 v8, v8, s60, v200
	v_mul_f32_e32 v7, v13, v173
	v_mov_b32_e32 v12, v167
	v_mul_f32_e32 v5, v149, v7
	v_med3_f32 v6, v14, s60, v200
	v_med3_f32 v7, v15, s60, v200
	v_med3_f32 v14, v16, s60, v200
	v_mov_b32_e32 v13, v167
	v_cvt_pk_fp8_f32 v12, v6, v8
	v_cvt_pk_fp8_f32 v13, v7, v14
	s_lshl_b32 s4, s36, 7
	s_or_b32 s4, s4, s54
	v_lshl_add_u32 v2, v4, 3, s4
	v_lshl_add_u32 v4, s62, 8, v11
	v_med3_f32 v15, v18, s60, v200
	v_med3_f32 v16, v17, s60, v200
	v_med3_f32 v6, v20, s60, v200
	v_med3_f32 v5, v5, s60, v200
	v_cvt_pk_fp8_f32 v12, v15, v6 op_sel:[0,0,1]
	v_cvt_pk_fp8_f32 v13, v16, v5 op_sel:[0,0,1]
	v_ashrrev_i32_e32 v5, 31, v4
	v_lshlrev_b64 v[6:7], 9, v[4:5]
	v_ashrrev_i32_e32 v3, 31, v2
	v_lshl_add_u64 v[6:7], s[18:19], 0, v[6:7]
	v_cndmask_b32_e64 v8, 0, 1, s[38:39]
	v_lshl_add_u64 v[6:7], v[6:7], 0, v[2:3]
	v_cmp_ne_u32_e64 s[4:5], 1, v8
	s_andn2_b64 vcc, exec, s[38:39]
	global_store_dwordx2 v[6:7], v[12:13], off
	s_cbranch_vccnz .LBB0_1052
	v_add3_u32 v8, s14, 16, v11
	s_waitcnt lgkmcnt(0)
	v_cmp_lt_i32_e32 vcc, v8, v10
	v_mov_b32_e32 v9, 0
	s_and_saveexec_b64 s[36:37], vcc
	s_cbranch_execz .LBB0_1051
	s_ashr_i32 s11, s10, 31
	s_lshl_b64 s[38:39], s[10:11], 15
	s_add_u32 s38, s51, s38
	s_addc_u32 s39, s52, s39
	v_ashrrev_i32_e32 v9, 31, v8
	v_lshl_add_u64 v[8:9], v[8:9], 2, s[38:39]
	s_waitcnt vmcnt(7)
	v_mul_f32_e32 v9, 0x3b800000, v247

.LBB0_1052:
	v_mul_f32_e32 v12, 0xbcb8aa3b, v142
	v_exp_f32_e32 v13, v12
	v_mul_f32_e32 v173, v142, v9
	v_mul_f32_e32 v8, 0xbcb8aa3b, v138
	v_add_f32_e32 v13, 1.0, v13
	v_rcp_f32_e32 v13, v13
	v_exp_f32_e32 v8, v8
	v_mul_f32_e32 v13, v13, v173
	v_add_f32_e32 v8, 1.0, v8
	v_mul_f32_e32 v16, v134, v13
	v_rcp_f32_e32 v13, v8
	v_mul_f32_e32 v173, v138, v9
	v_mul_f32_e32 v14, 0xbcb8aa3b, v143
	v_exp_f32_e32 v14, v14
	v_mul_f32_e32 v13, v13, v173
	v_mul_f32_e32 v173, v143, v9
	v_mul_f32_e32 v17, v130, v13
	v_add_f32_e32 v12, 1.0, v14
	v_rcp_f32_e32 v13, v12
	v_mul_f32_e32 v12, 0xbcb8aa3b, v139
	v_exp_f32_e32 v14, v12
	v_mul_f32_e32 v13, v13, v173
	v_mul_f32_e32 v173, v139, v9
	v_add_f32_e32 v8, 1.0, v14
	v_rcp_f32_e32 v15, v8
	v_mul_f32_e32 v19, v135, v13
	v_mul_f32_e32 v13, v15, v173
	v_mul_f32_e32 v14, 0xbcb8aa3b, v144
	v_exp_f32_e32 v14, v14
	v_mul_f32_e32 v173, v144, v9
	v_mul_f32_e32 v18, v131, v13
	v_add_f32_e32 v8, 1.0, v14
	v_rcp_f32_e32 v13, v8
	v_mul_f32_e32 v8, 0xbcb8aa3b, v140
	v_exp_f32_e32 v8, v8
	v_mul_f32_e32 v13, v13, v173
	v_mul_f32_e32 v173, v140, v9
	v_add_f32_e32 v8, 1.0, v8
	v_mul_f32_e32 v20, v136, v13
	v_rcp_f32_e32 v13, v8
	v_mul_f32_e32 v14, 0xbcb8aa3b, v145
	v_exp_f32_e32 v14, v14
	v_mul_f32_e32 v13, v13, v173
	v_mul_f32_e32 v21, v132, v13
	v_add_f32_e32 v12, 1.0, v14
	v_rcp_f32_e32 v13, v12
	v_mul_f32_e32 v12, 0xbcb8aa3b, v141
	v_exp_f32_e32 v14, v12
	v_mul_f32_e32 v173, v145, v9
	v_mul_f32_e32 v13, v13, v173
	v_add_f32_e32 v8, 1.0, v14
	v_rcp_f32_e32 v15, v8
	v_mul_f32_e32 v173, v141, v9
	v_mul_f32_e32 v12, v137, v13
	v_mul_f32_e32 v9, v15, v173
	v_med3_f32 v15, v19, s60, v200
	v_mul_f32_e32 v13, v133, v9
	v_med3_f32 v9, v16, s60, v200
	v_mov_b32_e32 v8, v167
	v_med3_f32 v14, v17, s60, v200
	v_med3_f32 v16, v18, s60, v200
	v_cvt_pk_fp8_f32 v8, v9, v15
	v_mov_b32_e32 v9, v167
	v_cvt_pk_fp8_f32 v9, v14, v16
	v_med3_f32 v17, v20, s60, v200
	v_med3_f32 v18, v21, s60, v200
	v_med3_f32 v12, v12, s60, v200
	v_med3_f32 v13, v13, s60, v200
	v_cvt_pk_fp8_f32 v8, v17, v12 op_sel:[0,0,1]
	v_cvt_pk_fp8_f32 v9, v18, v13 op_sel:[0,0,1]
	v_add_co_u32_e32 v6, vcc, 0x2000, v6
	s_nop 1
	v_addc_co_u32_e32 v7, vcc, 0, v7, vcc
	global_store_dwordx2 v[6:7], v[8:9], off
	v_mov_b32_e32 v9, 0x3b800000
	s_and_b64 vcc, exec, s[4:5]
	v_mov_b32_e32 v7, 0x3b800000
	s_cbranch_vccnz .LBB0_1056
	v_add3_u32 v6, s14, 32, v11
	s_waitcnt lgkmcnt(0)
	v_cmp_lt_i32_e32 vcc, v6, v10
	v_mov_b32_e32 v7, 0
	s_and_saveexec_b64 s[36:37], vcc
	s_cbranch_execz .LBB0_1055
	s_ashr_i32 s11, s10, 31
	s_lshl_b64 s[38:39], s[10:11], 15
	s_add_u32 s38, s51, s38
	s_addc_u32 s39, s52, s39
	v_ashrrev_i32_e32 v7, 31, v6
	v_lshl_add_u64 v[6:7], v[6:7], 2, s[38:39]
	s_waitcnt vmcnt(7)
	v_mul_f32_e32 v7, 0x3b800000, v248

.LBB0_1056:
	v_mul_f32_e32 v8, 0xbcb8aa3b, v126
	v_exp_f32_e32 v8, v8
	v_mul_f32_e32 v173, v126, v7
	v_mul_f32_e32 v6, 0xbcb8aa3b, v122
	v_add_f32_e32 v8, 1.0, v8
	v_rcp_f32_e32 v13, v8
	v_exp_f32_e32 v6, v6
	v_mul_f32_e32 v13, v13, v173
	v_add_f32_e32 v6, 1.0, v6
	v_mul_f32_e32 v8, v118, v13
	v_rcp_f32_e32 v13, v6
	v_mul_f32_e32 v173, v122, v7
	v_mul_f32_e32 v14, 0xbcb8aa3b, v127
	v_exp_f32_e32 v14, v14
	v_mul_f32_e32 v13, v13, v173
	v_mul_f32_e32 v173, v127, v7
	v_mul_f32_e32 v16, v114, v13
	v_add_f32_e32 v12, 1.0, v14
	v_rcp_f32_e32 v13, v12
	v_mul_f32_e32 v12, 0xbcb8aa3b, v123
	v_exp_f32_e32 v14, v12
	v_mul_f32_e32 v13, v13, v173
	v_mul_f32_e32 v173, v123, v7
	v_add_f32_e32 v6, 1.0, v14
	v_rcp_f32_e32 v15, v6
	v_mul_f32_e32 v18, v119, v13
	v_mul_f32_e32 v13, v15, v173
	v_mul_f32_e32 v14, 0xbcb8aa3b, v128
	v_exp_f32_e32 v14, v14
	v_mul_f32_e32 v173, v128, v7
	v_mul_f32_e32 v17, v115, v13
	v_add_f32_e32 v6, 1.0, v14
	v_rcp_f32_e32 v13, v6
	v_mul_f32_e32 v6, 0xbcb8aa3b, v124
	v_exp_f32_e32 v6, v6
	v_mul_f32_e32 v13, v13, v173
	v_mul_f32_e32 v173, v124, v7
	v_add_f32_e32 v6, 1.0, v6
	v_mul_f32_e32 v19, v120, v13
	v_rcp_f32_e32 v13, v6
	v_mul_f32_e32 v14, 0xbcb8aa3b, v129
	v_exp_f32_e32 v14, v14
	v_mul_f32_e32 v13, v13, v173
	v_mul_f32_e32 v20, v116, v13
	v_add_f32_e32 v12, 1.0, v14
	v_rcp_f32_e32 v13, v12
	v_mul_f32_e32 v12, 0xbcb8aa3b, v125
	v_exp_f32_e32 v14, v12
	v_mul_f32_e32 v173, v129, v7
	v_mul_f32_e32 v13, v13, v173
	v_add_f32_e32 v6, 1.0, v14
	v_rcp_f32_e32 v15, v6
	v_mul_f32_e32 v173, v125, v7
	v_mul_f32_e32 v22, v121, v13
	v_mul_f32_e32 v7, v15, v173
	v_med3_f32 v13, v18, s60, v200
	v_mul_f32_e32 v6, v117, v7
	v_med3_f32 v7, v8, s60, v200
	v_mov_b32_e32 v12, v167
	v_med3_f32 v8, v16, s60, v200
	v_med3_f32 v14, v17, s60, v200
	v_cvt_pk_fp8_f32 v12, v7, v13
	v_mov_b32_e32 v13, v167
	v_cvt_pk_fp8_f32 v13, v8, v14
	v_med3_f32 v15, v19, s60, v200
	v_med3_f32 v16, v20, s60, v200
	v_med3_f32 v7, v22, s60, v200
	v_med3_f32 v6, v6, s60, v200
	v_cvt_pk_fp8_f32 v12, v15, v7 op_sel:[0,0,1]
	v_cvt_pk_fp8_f32 v13, v16, v6 op_sel:[0,0,1]
	v_lshlrev_b64 v[6:7], 9, v[4:5]
	v_lshl_add_u64 v[6:7], s[18:19], 0, v[6:7]
	v_lshl_add_u64 v[6:7], v[6:7], 0, v[2:3]
	v_add_co_u32_e32 v14, vcc, 0x4000, v6
	s_nop 1
	v_addc_co_u32_e32 v15, vcc, 0, v7, vcc
	s_and_b64 vcc, exec, s[4:5]
	global_store_dwordx2 v[14:15], v[12:13], off
	s_cbranch_vccnz .LBB0_1060
	v_add3_u32 v8, s14, 48, v11
	s_waitcnt lgkmcnt(0)
	v_cmp_lt_i32_e32 vcc, v8, v10
	v_mov_b32_e32 v9, 0
	s_and_saveexec_b64 s[36:37], vcc
	s_cbranch_execz .LBB0_1059
	s_ashr_i32 s11, s10, 31
	s_lshl_b64 s[38:39], s[10:11], 15
	s_add_u32 s38, s51, s38
	s_addc_u32 s39, s52, s39
	v_ashrrev_i32_e32 v9, 31, v8
	v_lshl_add_u64 v[8:9], v[8:9], 2, s[38:39]
	s_waitcnt vmcnt(7)
	v_mul_f32_e32 v9, 0x3b800000, v249

.LBB0_1060:
	v_mul_f32_e32 v12, 0xbcb8aa3b, v110
	v_exp_f32_e32 v13, v12
	v_mul_f32_e32 v173, v110, v9
	v_mul_f32_e32 v8, 0xbcb8aa3b, v106
	v_add_f32_e32 v13, 1.0, v13
	v_rcp_f32_e32 v13, v13
	v_exp_f32_e32 v8, v8
	v_mul_f32_e32 v13, v13, v173
	v_add_f32_e32 v8, 1.0, v8
	v_mul_f32_e32 v16, v102, v13
	v_rcp_f32_e32 v13, v8
	v_mul_f32_e32 v173, v106, v9
	v_mul_f32_e32 v14, 0xbcb8aa3b, v111
	v_exp_f32_e32 v14, v14
	v_mul_f32_e32 v13, v13, v173
	v_mul_f32_e32 v173, v111, v9
	v_mul_f32_e32 v17, v98, v13
	v_add_f32_e32 v12, 1.0, v14
	v_rcp_f32_e32 v13, v12
	v_mul_f32_e32 v12, 0xbcb8aa3b, v107
	v_exp_f32_e32 v14, v12
	v_mul_f32_e32 v13, v13, v173
	v_mul_f32_e32 v173, v107, v9
	v_add_f32_e32 v8, 1.0, v14
	v_rcp_f32_e32 v15, v8
	v_mul_f32_e32 v19, v103, v13
	v_mul_f32_e32 v13, v15, v173
	v_mul_f32_e32 v14, 0xbcb8aa3b, v112
	v_exp_f32_e32 v14, v14
	v_mul_f32_e32 v173, v112, v9
	v_mul_f32_e32 v18, v99, v13
	v_add_f32_e32 v8, 1.0, v14
	v_rcp_f32_e32 v13, v8
	v_mul_f32_e32 v8, 0xbcb8aa3b, v108
	v_exp_f32_e32 v8, v8
	v_mul_f32_e32 v13, v13, v173
	v_mul_f32_e32 v173, v108, v9
	v_add_f32_e32 v8, 1.0, v8
	v_mul_f32_e32 v20, v104, v13
	v_rcp_f32_e32 v13, v8
	v_mul_f32_e32 v14, 0xbcb8aa3b, v113
	v_exp_f32_e32 v14, v14
	v_mul_f32_e32 v13, v13, v173
	v_mul_f32_e32 v21, v100, v13
	v_add_f32_e32 v12, 1.0, v14
	v_rcp_f32_e32 v13, v12
	v_mul_f32_e32 v12, 0xbcb8aa3b, v109
	v_exp_f32_e32 v14, v12
	v_mul_f32_e32 v173, v113, v9
	v_mul_f32_e32 v13, v13, v173
	v_add_f32_e32 v8, 1.0, v14
	v_rcp_f32_e32 v15, v8
	v_mul_f32_e32 v173, v109, v9
	v_mul_f32_e32 v12, v105, v13
	v_mul_f32_e32 v9, v15, v173
	v_med3_f32 v15, v19, s60, v200
	v_mul_f32_e32 v13, v101, v9
	v_med3_f32 v9, v16, s60, v200
	v_mov_b32_e32 v8, v167
	v_med3_f32 v14, v17, s60, v200
	v_med3_f32 v16, v18, s60, v200
	v_cvt_pk_fp8_f32 v8, v9, v15
	v_mov_b32_e32 v9, v167
	v_cvt_pk_fp8_f32 v9, v14, v16
	v_med3_f32 v17, v20, s60, v200
	v_med3_f32 v18, v21, s60, v200
	v_med3_f32 v12, v12, s60, v200
	v_med3_f32 v13, v13, s60, v200
	v_cvt_pk_fp8_f32 v8, v17, v12 op_sel:[0,0,1]
	v_cvt_pk_fp8_f32 v9, v18, v13 op_sel:[0,0,1]
	v_add_co_u32_e32 v6, vcc, 0x6000, v6
	s_nop 1
	v_addc_co_u32_e32 v7, vcc, 0, v7, vcc
	global_store_dwordx2 v[6:7], v[8:9], off
	v_mov_b32_e32 v9, 0x3b800000
	s_and_b64 vcc, exec, s[4:5]
	v_mov_b32_e32 v7, 0x3b800000
	s_cbranch_vccnz .LBB0_1064
	s_add_i32 s11, s14, 0x80
	v_add_u32_e32 v6, s11, v11
	s_waitcnt lgkmcnt(0)
	v_cmp_lt_i32_e32 vcc, v6, v10
	v_mov_b32_e32 v7, 0
	s_and_saveexec_b64 s[36:37], vcc
	s_cbranch_execz .LBB0_1063
	s_ashr_i32 s11, s10, 31
	s_lshl_b64 s[38:39], s[10:11], 15
	s_add_u32 s38, s51, s38
	s_addc_u32 s39, s52, s39
	v_ashrrev_i32_e32 v7, 31, v6
	v_lshl_add_u64 v[6:7], v[6:7], 2, s[38:39]
	s_waitcnt vmcnt(7)
	v_mul_f32_e32 v7, 0x3b800000, v250

.LBB0_1064:
	v_mul_f32_e32 v8, 0xbcb8aa3b, v94
	v_exp_f32_e32 v8, v8
	v_mul_f32_e32 v173, v94, v7
	v_mul_f32_e32 v6, 0xbcb8aa3b, v90
	v_add_f32_e32 v8, 1.0, v8
	v_rcp_f32_e32 v13, v8
	v_exp_f32_e32 v6, v6
	v_mul_f32_e32 v13, v13, v173
	v_add_f32_e32 v6, 1.0, v6
	v_mul_f32_e32 v8, v86, v13
	v_rcp_f32_e32 v13, v6
	v_mul_f32_e32 v173, v90, v7
	v_mul_f32_e32 v14, 0xbcb8aa3b, v95
	v_exp_f32_e32 v14, v14
	v_mul_f32_e32 v13, v13, v173
	v_mul_f32_e32 v173, v95, v7
	v_mul_f32_e32 v16, v82, v13
	v_add_f32_e32 v12, 1.0, v14
	v_rcp_f32_e32 v13, v12
	v_mul_f32_e32 v12, 0xbcb8aa3b, v91
	v_exp_f32_e32 v14, v12
	v_mul_f32_e32 v13, v13, v173
	v_mul_f32_e32 v173, v91, v7
	v_add_f32_e32 v6, 1.0, v14
	v_rcp_f32_e32 v15, v6
	v_mul_f32_e32 v18, v87, v13
	v_mul_f32_e32 v13, v15, v173
	v_mul_f32_e32 v14, 0xbcb8aa3b, v96
	v_exp_f32_e32 v14, v14
	v_mul_f32_e32 v173, v96, v7
	v_mul_f32_e32 v17, v83, v13
	v_add_f32_e32 v6, 1.0, v14
	v_rcp_f32_e32 v13, v6
	v_mul_f32_e32 v6, 0xbcb8aa3b, v92
	v_exp_f32_e32 v6, v6
	v_mul_f32_e32 v13, v13, v173
	v_mul_f32_e32 v173, v92, v7
	v_add_f32_e32 v6, 1.0, v6
	v_mul_f32_e32 v19, v88, v13
	v_rcp_f32_e32 v13, v6
	v_mul_f32_e32 v14, 0xbcb8aa3b, v97
	v_exp_f32_e32 v14, v14
	v_mul_f32_e32 v13, v13, v173
	v_mul_f32_e32 v20, v84, v13
	v_add_f32_e32 v12, 1.0, v14
	v_rcp_f32_e32 v13, v12
	v_mul_f32_e32 v12, 0xbcb8aa3b, v93
	v_exp_f32_e32 v14, v12
	v_mul_f32_e32 v173, v97, v7
	v_mul_f32_e32 v13, v13, v173
	v_add_f32_e32 v6, 1.0, v14
	v_rcp_f32_e32 v15, v6
	v_mul_f32_e32 v173, v93, v7
	v_mul_f32_e32 v22, v89, v13
	v_mul_f32_e32 v7, v15, v173
	v_med3_f32 v13, v18, s60, v200
	v_mul_f32_e32 v6, v85, v7
	v_med3_f32 v7, v8, s60, v200
	v_mov_b32_e32 v12, v167
	v_med3_f32 v8, v16, s60, v200
	v_med3_f32 v14, v17, s60, v200
	v_cvt_pk_fp8_f32 v12, v7, v13
	v_mov_b32_e32 v13, v167
	v_cvt_pk_fp8_f32 v13, v8, v14
	v_med3_f32 v15, v19, s60, v200
	v_med3_f32 v16, v20, s60, v200
	v_med3_f32 v7, v22, s60, v200
	v_med3_f32 v6, v6, s60, v200
	v_cvt_pk_fp8_f32 v12, v15, v7 op_sel:[0,0,1]
	v_cvt_pk_fp8_f32 v13, v16, v6 op_sel:[0,0,1]
	v_lshlrev_b64 v[6:7], 9, v[4:5]
	v_lshl_add_u64 v[6:7], s[18:19], 0, v[6:7]
	v_lshl_add_u64 v[6:7], v[6:7], 0, v[2:3]
	v_add_co_u32_e32 v14, vcc, 0x10000, v6
	s_nop 1
	v_addc_co_u32_e32 v15, vcc, 0, v7, vcc
	s_and_b64 vcc, exec, s[4:5]
	global_store_dwordx2 v[14:15], v[12:13], off
	s_cbranch_vccnz .LBB0_1068
	s_add_i32 s11, s14, 0x90
	v_add_u32_e32 v8, s11, v11
	s_waitcnt lgkmcnt(0)
	v_cmp_lt_i32_e32 vcc, v8, v10
	v_mov_b32_e32 v9, 0
	s_and_saveexec_b64 s[36:37], vcc
	s_cbranch_execz .LBB0_1067
	s_ashr_i32 s11, s10, 31
	s_lshl_b64 s[38:39], s[10:11], 15
	s_add_u32 s38, s51, s38
	s_addc_u32 s39, s52, s39
	v_ashrrev_i32_e32 v9, 31, v8
	v_lshl_add_u64 v[8:9], v[8:9], 2, s[38:39]
	s_waitcnt vmcnt(7)
	v_mul_f32_e32 v9, 0x3b800000, v251

.LBB0_1068:
	v_mul_f32_e32 v12, 0xbcb8aa3b, v78
	v_exp_f32_e32 v13, v12
	v_mul_f32_e32 v173, v78, v9
	v_mul_f32_e32 v8, 0xbcb8aa3b, v74
	v_add_f32_e32 v13, 1.0, v13
	v_rcp_f32_e32 v13, v13
	v_exp_f32_e32 v8, v8
	v_mul_f32_e32 v13, v13, v173
	v_add_f32_e32 v8, 1.0, v8
	v_mul_f32_e32 v16, v70, v13
	v_rcp_f32_e32 v13, v8
	v_mul_f32_e32 v173, v74, v9
	v_mul_f32_e32 v14, 0xbcb8aa3b, v79
	v_exp_f32_e32 v14, v14
	v_mul_f32_e32 v13, v13, v173
	v_mul_f32_e32 v173, v79, v9
	v_mul_f32_e32 v17, v66, v13
	v_add_f32_e32 v12, 1.0, v14
	v_rcp_f32_e32 v13, v12
	v_mul_f32_e32 v12, 0xbcb8aa3b, v75
	v_exp_f32_e32 v14, v12
	v_mul_f32_e32 v13, v13, v173
	v_mul_f32_e32 v173, v75, v9
	v_add_f32_e32 v8, 1.0, v14
	v_rcp_f32_e32 v15, v8
	v_mul_f32_e32 v19, v71, v13
	v_mul_f32_e32 v13, v15, v173
	v_mul_f32_e32 v14, 0xbcb8aa3b, v80
	v_exp_f32_e32 v14, v14
	v_mul_f32_e32 v173, v80, v9
	v_mul_f32_e32 v18, v67, v13
	v_add_f32_e32 v8, 1.0, v14
	v_rcp_f32_e32 v13, v8
	v_mul_f32_e32 v8, 0xbcb8aa3b, v76
	v_exp_f32_e32 v8, v8
	v_mul_f32_e32 v13, v13, v173
	v_mul_f32_e32 v173, v76, v9
	v_add_f32_e32 v8, 1.0, v8
	v_mul_f32_e32 v20, v72, v13
	v_rcp_f32_e32 v13, v8
	v_mul_f32_e32 v14, 0xbcb8aa3b, v81
	v_exp_f32_e32 v14, v14
	v_mul_f32_e32 v13, v13, v173
	v_mul_f32_e32 v21, v68, v13
	v_add_f32_e32 v12, 1.0, v14
	v_rcp_f32_e32 v13, v12
	v_mul_f32_e32 v12, 0xbcb8aa3b, v77
	v_exp_f32_e32 v14, v12
	v_mul_f32_e32 v173, v81, v9
	v_mul_f32_e32 v13, v13, v173
	v_add_f32_e32 v8, 1.0, v14
	v_rcp_f32_e32 v15, v8
	v_mul_f32_e32 v173, v77, v9
	v_mul_f32_e32 v12, v73, v13
	v_mul_f32_e32 v9, v15, v173
	v_med3_f32 v15, v19, s60, v200
	v_mul_f32_e32 v13, v69, v9
	v_med3_f32 v9, v16, s60, v200
	v_mov_b32_e32 v8, v167
	v_med3_f32 v14, v17, s60, v200
	v_med3_f32 v16, v18, s60, v200
	v_cvt_pk_fp8_f32 v8, v9, v15
	v_mov_b32_e32 v9, v167
	v_cvt_pk_fp8_f32 v9, v14, v16
	v_med3_f32 v17, v20, s60, v200
	v_med3_f32 v18, v21, s60, v200
	v_med3_f32 v12, v12, s60, v200
	v_med3_f32 v13, v13, s60, v200
	v_cvt_pk_fp8_f32 v8, v17, v12 op_sel:[0,0,1]
	v_cvt_pk_fp8_f32 v9, v18, v13 op_sel:[0,0,1]
	v_add_co_u32_e32 v6, vcc, 0x12000, v6
	s_nop 1
	v_addc_co_u32_e32 v7, vcc, 0, v7, vcc
	global_store_dwordx2 v[6:7], v[8:9], off
	v_mov_b32_e32 v8, 0x3b800000
	s_and_b64 vcc, exec, s[4:5]
	v_mov_b32_e32 v7, 0x3b800000
	s_cbranch_vccnz .LBB0_1072
	s_add_i32 s11, s14, 0xa0
	v_add_u32_e32 v6, s11, v11
	s_waitcnt lgkmcnt(0)
	v_cmp_lt_i32_e32 vcc, v6, v10
	v_mov_b32_e32 v7, 0
	s_and_saveexec_b64 s[36:37], vcc
	s_cbranch_execz .LBB0_1071
	s_ashr_i32 s11, s10, 31
	s_lshl_b64 s[38:39], s[10:11], 15
	s_add_u32 s38, s51, s38
	s_addc_u32 s39, s52, s39
	v_ashrrev_i32_e32 v7, 31, v6
	v_lshl_add_u64 v[6:7], v[6:7], 2, s[38:39]
	s_waitcnt vmcnt(7)
	v_mul_f32_e32 v7, 0x3b800000, v252

.LBB0_1072:
	v_mul_f32_e32 v9, 0xbcb8aa3b, v54
	v_exp_f32_e32 v9, v9
	v_mul_f32_e32 v173, v54, v7
	v_mul_f32_e32 v6, 0xbcb8aa3b, v50
	v_add_f32_e32 v9, 1.0, v9
	v_rcp_f32_e32 v13, v9
	v_exp_f32_e32 v6, v6
	v_mul_f32_e32 v13, v13, v173
	v_add_f32_e32 v6, 1.0, v6
	v_mul_f32_e32 v9, v62, v13
	v_rcp_f32_e32 v13, v6
	v_mul_f32_e32 v173, v50, v7
	v_mul_f32_e32 v14, 0xbcb8aa3b, v55
	v_exp_f32_e32 v14, v14
	v_mul_f32_e32 v13, v13, v173
	v_mul_f32_e32 v173, v55, v7
	v_mul_f32_e32 v16, v58, v13
	v_add_f32_e32 v12, 1.0, v14
	v_rcp_f32_e32 v13, v12
	v_mul_f32_e32 v12, 0xbcb8aa3b, v51
	v_exp_f32_e32 v14, v12
	v_mul_f32_e32 v13, v13, v173
	v_mul_f32_e32 v173, v51, v7
	v_add_f32_e32 v6, 1.0, v14
	v_rcp_f32_e32 v15, v6
	v_mul_f32_e32 v18, v63, v13
	v_mul_f32_e32 v13, v15, v173
	v_mul_f32_e32 v14, 0xbcb8aa3b, v56
	v_exp_f32_e32 v14, v14
	v_mul_f32_e32 v173, v56, v7
	v_mul_f32_e32 v17, v59, v13
	v_add_f32_e32 v6, 1.0, v14
	v_rcp_f32_e32 v13, v6
	v_mul_f32_e32 v6, 0xbcb8aa3b, v52
	v_exp_f32_e32 v6, v6
	v_mul_f32_e32 v13, v13, v173
	v_mul_f32_e32 v173, v52, v7
	v_add_f32_e32 v6, 1.0, v6
	v_mul_f32_e32 v19, v64, v13
	v_rcp_f32_e32 v13, v6
	v_mul_f32_e32 v14, 0xbcb8aa3b, v57
	v_exp_f32_e32 v14, v14
	v_mul_f32_e32 v13, v13, v173
	v_mul_f32_e32 v20, v60, v13
	v_add_f32_e32 v12, 1.0, v14
	v_rcp_f32_e32 v13, v12
	v_mul_f32_e32 v12, 0xbcb8aa3b, v53
	v_exp_f32_e32 v14, v12
	v_mul_f32_e32 v173, v57, v7
	v_mul_f32_e32 v13, v13, v173
	v_add_f32_e32 v6, 1.0, v14
	v_rcp_f32_e32 v15, v6
	v_mul_f32_e32 v173, v53, v7
	v_mul_f32_e32 v12, v65, v13
	v_mul_f32_e32 v7, v15, v173
	v_med3_f32 v14, v18, s60, v200
	v_mul_f32_e32 v13, v61, v7
	v_med3_f32 v7, v9, s60, v200
	v_mov_b32_e32 v6, v167
	v_med3_f32 v9, v16, s60, v200
	v_med3_f32 v15, v17, s60, v200
	v_cvt_pk_fp8_f32 v6, v7, v14
	v_mov_b32_e32 v7, v167
	v_cvt_pk_fp8_f32 v7, v9, v15
	v_lshlrev_b64 v[4:5], 9, v[4:5]
	v_med3_f32 v16, v19, s60, v200
	v_med3_f32 v17, v20, s60, v200
	v_med3_f32 v9, v12, s60, v200
	v_med3_f32 v12, v13, s60, v200
	v_lshl_add_u64 v[4:5], s[18:19], 0, v[4:5]
	v_cvt_pk_fp8_f32 v6, v16, v9 op_sel:[0,0,1]
	v_cvt_pk_fp8_f32 v7, v17, v12 op_sel:[0,0,1]
	v_lshl_add_u64 v[2:3], v[4:5], 0, v[2:3]
	v_add_co_u32_e32 v4, vcc, 0x14000, v2
	s_nop 1
	v_addc_co_u32_e32 v5, vcc, 0, v3, vcc
	s_and_b64 vcc, exec, s[4:5]
	global_store_dwordx2 v[4:5], v[6:7], off
	s_cbranch_vccnz .LBB0_1076
	s_add_i32 s4, s14, 0xb0
	v_add_u32_e32 v4, s4, v11
	s_waitcnt lgkmcnt(0)
	v_cmp_lt_i32_e32 vcc, v4, v10
	v_mov_b32_e32 v8, 0
	s_and_saveexec_b64 s[4:5], vcc
	s_cbranch_execz .LBB0_1075
	s_ashr_i32 s11, s10, 31
	s_lshl_b64 s[10:11], s[10:11], 15
	s_add_u32 s10, s51, s10
	s_addc_u32 s11, s52, s11
	v_ashrrev_i32_e32 v5, 31, v4
	v_lshl_add_u64 v[4:5], v[4:5], 2, s[10:11]
	s_waitcnt vmcnt(7)
	v_mul_f32_e32 v8, 0x3b800000, v253
